# scan C: read-once record/state loads marked nt
# speedup vs baseline: 1.0054x; 1.0040x over previous
; #define GAS __attribute__((address_space(1)))
; DI void scanc_load(ScanCIn& o, const unsigned char* ws, GAS unsigned* flags, int item, int r16, int g, int l) {
;     asm volatile("" : "+s"(item));
;     const int u = item >> 2, it = item & 3; const int bh = u & 31, c = u >> 5; const size_t ui = (size_t)(bh * 128 + c);
;     {
;       GAS unsigned* fw = flags + 64 * bh; const unsigned need = 4u * ((unsigned)(c >> 2) + 1u); unsigned spins = 0;
;       while ((unsigned)__builtin_amdgcn_readfirstlane((int)__hip_atomic_load(fw, __ATOMIC_RELAXED, __HIP_MEMORY_SCOPE_AGENT)) < need) { __builtin_amdgcn_s_sleep(24); if (++spins > (1u << 20)) break; }
;       asm volatile("" ::: "memory"); }
;     const unsigned char* rec1 = ws + WS_SC1 + ui * U1_BYTES; const unsigned char* rec2 = ws + WS_SC2 + ui * U2_BYTES;
;     const __amdgpu_buffer_rsrc_t srs = __builtin_amdgcn_make_buffer_rsrc((void*)(ws + WS_SCT + ui * 8192), 0, 8192, 0x00020000);
; #pragma unroll
;     for (int s = 0; s < 2; ++s) o.ra[s] = *(const bf16x8*)(rec1 + U_RPP + (size_t)((16 * it + r16) * 64 + 32 * s + 8 * g) * 2);
; #pragma unroll
;     for (int vt = 0; vt < 4; ++vt) { { const u32x2 yw = *(const u32x2*)(rec2 + U_YLT + (size_t)((16 * it + r16) * 64 + 32 * (vt >> 1) + 8 * g + 4 * (vt & 1)) * 2); o.yl[vt] = (f32x4){bflo(yw.x), bfhi(yw.x), bflo(yw.y), bfhi(yw.y)}; }
;         const int vrow = 32 * (vt >> 1) + 8 * (r16 >> 2) + 4 * (vt & 1) + (r16 & 3);
; #pragma unroll
;         for (int s = 0; s < 2; ++s) o.sb[vt][s] = __builtin_bit_cast(bf16x8, __builtin_amdgcn_raw_buffer_load_b128(srs, (int)((vrow * 64 + 32 * s + 8 * g) * 2), 0, 16)); }
;     { const bf16_t* SIr = (const bf16_t*)(ws + WS_SIR); const bf16_t* SIk = (const bf16_t*)(ws + WS_SIK); const bf16_t* V = (const bf16_t*)(ws + (l > 0 ? WS_V1 : WS_VF)); const bf16_t* Gb = (const bf16_t*)(ws + WS_G);
;       const int b = bh >> 3, h = bh & 7; const size_t o0 = ((size_t)b * SEQ + c * 64 + 16 * it + r16) * CW + h * 64 + 8 * g;
; #pragma unroll
;       for (int p = 0; p < 2; ++p) { o.pr[p] = *(const u32x4*)(SIr + o0 + 32 * p); o.pk[p] = *(const u32x4*)(SIk + o0 + 32 * p); o.pv[p] = *(const u32x4*)(V + o0 + 32 * p); o.pg[p] = *(const u32x4*)(Gb + o0 + 32 * p); } }
; DI void scanc_item(const ScanCIn& o, Frame& F, int l, int item, int r16, int g) {
;     ...
;     for (int vt = 0; vt < 4; ++vt) { y[vt] = o.yl[vt];
; #pragma unroll
.LBB0_1231:
	v_readlane_b32 s0, v252, 19
	s_lshl_b32 s19, s0, 3
	v_readlane_b32 s1, v252, 20
	s_addk_i32 s19, 0xff00
	s_and_b64 s[0:1], s[40:41], exec
	v_readlane_b32 s0, v252, 11
	v_readlane_b32 s2, v252, 13
	v_readlane_b32 s1, v252, 12
	s_cselect_b32 s8, s2, 0x1a200000
	s_add_u32 s0, s94, 0x10200000
	s_addc_u32 s1, s95, 0
	v_readlane_b32 s3, v252, 14
	s_add_u32 s2, s94, 0x14200000
	s_addc_u32 s3, s95, 0
	s_add_u32 s6, s94, 0x1c200000
	s_addc_u32 s7, s95, 0
	s_add_u32 s8, s94, s8
	s_addc_u32 s9, s95, 0
	s_add_u32 s10, s94, 0x7200000
	s_addc_u32 s11, s95, 0
	s_lshl_b32 s15, s15, 6
	s_and_b32 s44, s15, 0x1c0
	s_lshl_b32 s15, s12, 10
	s_lshl_b32 s16, s13, 6
	s_and_b32 s15, s15, 0x6000
	s_ashr_i32 s17, s16, 31
	s_add_u32 s15, s15, s16
	s_addc_u32 s16, 0, s17
	s_and_b32 s17, s14, 3
	s_lshl_b32 s12, s12, 7
	s_lshl_b32 s14, s17, 4
	s_add_i32 s12, s12, s13
	v_and_b32_e32 v64, 15, v196
	s_or_b32 s14, s15, s14
	s_ashr_i32 s13, s12, 31
	v_or_b32_e32 v2, s14, v64
	s_lshl_b64 s[14:15], s[12:13], 13
	v_readlane_b32 s28, v252, 7
	v_ashrrev_i32_e32 v0, 1, v196
	s_add_u32 s28, s22, s14
	v_and_b32_e32 v194, -8, v0
	v_readlane_b32 s29, v252, 8
	s_addc_u32 s14, s23, s15
	v_lshl_add_u32 v197, v64, 6, v194
	s_and_b32 s29, s14, 0xffff
	s_lshl_b64 s[12:13], s[12:13], 14
	s_add_u32 s14, s94, s12
	v_lshl_add_u32 v4, s17, 10, v197
	v_lshlrev_b32_e32 v0, 1, v196
	v_and_b32_e32 v1, 3, v196
	s_addc_u32 s15, s95, s13
	v_ashrrev_i32_e32 v5, 31, v4
	v_and_or_b32 v0, v0, 24, v1
	v_and_b32_e32 v1, -16, v196
	v_ashrrev_i32_e32 v195, 31, v194
	v_mov_b32_e32 v3, s16
	s_add_u32 s12, s14, 0x16202000
	v_lshlrev_b64 v[4:5], 1, v[4:5]
	v_lshl_add_u32 v198, v0, 7, v1
	v_lshl_add_u64 v[0:1], s[44:45], 0, v[194:195]
	v_lshlrev_b64 v[2:3], 9, v[2:3]
	s_addc_u32 s13, s15, 0
	v_lshl_add_u64 v[6:7], v[4:5], 0, 64
	v_lshl_add_u64 v[0:1], v[0:1], 0, v[2:3]
	v_lshl_add_u64 v[8:9], s[12:13], 0, v[6:7]
	v_lshlrev_b64 v[0:1], 1, v[0:1]
	global_load_dwordx4 v[16:19], v[8:9], off nt
	v_lshl_add_u64 v[2:3], s[0:1], 0, v[0:1]
	v_lshl_add_u64 v[8:9], s[2:3], 0, v[0:1]
	v_add_u32_e32 v199, 0x1000, v198
	v_readlane_b32 s30, v252, 9
	v_readlane_b32 s31, v252, 10
	global_load_dwordx4 v[74:77], v[2:3], off nt
	global_load_dwordx4 v[86:89], v[2:3], off offset:64 nt
	global_load_dwordx4 v[78:81], v[8:9], off nt
	global_load_dwordx4 v[90:93], v[8:9], off offset:64 nt
	v_lshl_add_u64 v[2:3], s[6:7], 0, v[0:1]
	v_lshl_add_u64 v[8:9], s[12:13], 0, v[4:5]
	global_load_dwordx4 v[32:35], v[8:9], off nt
	v_lshl_add_u64 v[0:1], s[8:9], 0, v[0:1]
	global_load_dwordx4 v[118:121], v[2:3], off offset:64 nt
	global_load_dwordx4 v[94:97], v[2:3], off nt
	global_load_dwordx4 v[114:117], v[0:1], off offset:64 nt
	global_load_dwordx4 v[98:101], v[0:1], off nt
	buffer_load_dwordx4 v[66:69], v199, s[28:31], 0 offen offset:576 sc1
	buffer_load_dwordx4 v[52:55], v199, s[28:31], 0 offen offset:512 sc1
	buffer_load_dwordx4 v[44:47], v199, s[28:31], 0 offen offset:64 sc1
	buffer_load_dwordx4 v[40:43], v199, s[28:31], 0 offen sc1
	buffer_load_dwordx4 v[28:31], v198, s[28:31], 0 offen offset:576 sc1
	buffer_load_dwordx4 v[24:27], v198, s[28:31], 0 offen offset:512 sc1
	buffer_load_dwordx4 v[8:11], v198, s[28:31], 0 offen offset:64 sc1
	s_add_u32 s12, s14, 0x1e202000
	s_addc_u32 s13, s15, 0
	v_lshl_add_u64 v[0:1], s[12:13], 0, v[6:7]
	v_lshl_add_u64 v[2:3], s[12:13], 0, v[4:5]
	buffer_load_dwordx4 v[12:15], v198, s[28:31], 0 offen sc1
	global_load_dwordx4 v[4:7], v[0:1], off nt
	s_nop 0
	global_load_dwordx4 v[0:3], v[2:3], off nt
	s_mov_b64 s[26:27], s[30:31]
	v_writelane_b32 v252, s24, 7
	v_add_u32_e32 v200, 64, v198
	v_add_u32_e32 v201, 0x200, v198
	v_writelane_b32 v252, s25, 8
	v_writelane_b32 v252, s26, 9
	v_writelane_b32 v252, s27, 10
	v_add_u32_e32 v206, 0x240, v198
	v_add_u32_e32 v207, 0x1040, v198
	v_add_u32_e32 v208, 0x1200, v198
	v_add_u32_e32 v209, 0x1240, v198
	v_lshl_add_u32 v210, v194, 2, s83
	s_waitcnt vmcnt(19)
	v_lshlrev_b32_e32 v50, 16, v17
	v_and_b32_e32 v51, 0xffff0000, v17
	v_and_b32_e32 v17, 64, v230
	v_lshlrev_b32_e32 v48, 16, v16
	v_and_b32_e32 v49, 0xffff0000, v16
	v_xor_b32_e32 v16, 16, v230
	v_add_u32_e32 v17, 64, v17
	v_cmp_lt_i32_e32 vcc, v16, v17
	v_lshlrev_b32_e32 v82, 16, v18
	v_and_b32_e32 v83, 0xffff0000, v18
	v_cndmask_b32_e32 v16, v230, v16, vcc
	v_lshlrev_b32_e32 v211, 2, v16
	v_xor_b32_e32 v16, 32, v230
	v_cmp_lt_i32_e32 vcc, v16, v17
	v_lshlrev_b32_e32 v84, 16, v19
	v_and_b32_e32 v85, 0xffff0000, v19
	v_cndmask_b32_e32 v16, v230, v16, vcc
	s_waitcnt vmcnt(14)
	v_lshlrev_b32_e32 v36, 16, v34
	v_and_b32_e32 v37, 0xffff0000, v34
	v_lshlrev_b32_e32 v38, 16, v35
	v_and_b32_e32 v39, 0xffff0000, v35
	v_lshlrev_b32_e32 v20, 16, v32
	v_and_b32_e32 v21, 0xffff0000, v32
	v_lshlrev_b32_e32 v22, 16, v33
	v_and_b32_e32 v23, 0xffff0000, v33
	v_lshlrev_b32_e32 v212, 2, v16
	s_branch .LBB0_1235
; DI float bflo(unsigned w) { return __uint_as_float(w << 16); }
; DI float bfhi(unsigned w) { return __uint_as_float(w & 0xffff0000u); }
; DI void scanc_load(ScanCIn& o, const unsigned char* ws, GAS unsigned* flags, int item, int r16, int g, int l) {
;     ...
;     const unsigned char* rec1 = ws + WS_SC1 + ui * U1_BYTES; const unsigned char* rec2 = ws + WS_SC2 + ui * U2_BYTES;
;     const __amdgpu_buffer_rsrc_t srs = __builtin_amdgcn_make_buffer_rsrc((void*)(ws + WS_SCT + ui * 8192), 0, 8192, 0x00020000);
; #pragma unroll
;     for (int s = 0; s < 2; ++s) o.ra[s] = *(const bf16x8*)(rec1 + U_RPP + (size_t)((16 * it + r16) * 64 + 32 * s + 8 * g) * 2);
; #pragma unroll
;     for (int vt = 0; vt < 4; ++vt) { { const u32x2 yw = *(const u32x2*)(rec2 + U_YLT + (size_t)((16 * it + r16) * 64 + 32 * (vt >> 1) + 8 * g + 4 * (vt & 1)) * 2); o.yl[vt] = (f32x4){bflo(yw.x), bfhi(yw.x), bflo(yw.y), bfhi(yw.y)}; }
;         const int vrow = 32 * (vt >> 1) + 8 * (r16 >> 2) + 4 * (vt & 1) + (r16 & 3);
; #pragma unroll
;         for (int s = 0; s < 2; ++s) o.sb[vt][s] = __builtin_bit_cast(bf16x8, __builtin_amdgcn_raw_buffer_load_b128(srs, (int)((vrow * 64 + 32 * s + 8 * g) * 2), 0, 16)); }
;     { const bf16_t* SIr = (const bf16_t*)(ws + WS_SIR); const bf16_t* SIk = (const bf16_t*)(ws + WS_SIK); const bf16_t* V = (const bf16_t*)(ws + (l > 0 ? WS_V1 : WS_VF)); const bf16_t* Gb = (const bf16_t*)(ws + WS_G);
;       const int b = bh >> 3, h = bh & 7; const size_t o0 = ((size_t)b * SEQ + c * 64 + 16 * it + r16) * CW + h * 64 + 8 * g;
; #pragma unroll
;       for (int p = 0; p < 2; ++p) { o.pr[p] = *(const u32x4*)(SIr + o0 + 32 * p); o.pk[p] = *(const u32x4*)(SIk + o0 + 32 * p); o.pv[p] = *(const u32x4*)(V + o0 + 32 * p); o.pg[p] = *(const u32x4*)(Gb + o0 + 32 * p); } }
.LBB0_1232:
	s_lshl_b32 s12, s26, 7
	s_add_i32 s12, s12, s25
	s_ashr_i32 s13, s12, 31
	s_and_b32 s27, s27, 3
	s_lshl_b64 s[14:15], s[12:13], 14
	s_add_u32 s14, s94, s14
	s_addc_u32 s15, s95, s15
	s_lshl_b64 s[12:13], s[12:13], 13
	v_readlane_b32 s36, v252, 7
	s_add_u32 s36, s22, s12
	v_lshl_add_u32 v0, s27, 10, v197
	s_addc_u32 s28, s23, s13
	v_ashrrev_i32_e32 v1, 31, v0
	v_readlane_b32 s37, v252, 8
	s_add_u32 s12, s14, 0x1e202000
	v_lshlrev_b64 v[8:9], 1, v[0:1]
	s_addc_u32 s13, s15, 0
	v_lshl_add_u64 v[40:41], v[8:9], 0, 64
	s_and_b32 s37, s28, 0xffff
	v_lshl_add_u64 v[0:1], s[12:13], 0, v[8:9]
	v_lshl_add_u64 v[4:5], s[12:13], 0, v[40:41]
	s_add_u32 s12, s14, 0x16202000
	s_addc_u32 s13, s15, 0
	v_lshl_add_u64 v[8:9], s[12:13], 0, v[8:9]
	global_load_dwordx4 v[22:25], v[8:9], off nt
	v_readlane_b32 s38, v252, 9
	v_readlane_b32 s39, v252, 10
	v_lshl_add_u64 v[40:41], s[12:13], 0, v[40:41]
	global_load_dwordx4 v[0:3], v[0:1], off nt
	s_mov_b64 s[14:15], s[38:39]
	global_load_dwordx4 v[4:7], v[4:5], off nt
	s_nop 0
	buffer_load_dwordx4 v[12:15], v198, s[36:39], 0 offen sc1
	buffer_load_dwordx4 v[8:11], v200, s[36:39], 0 offen sc1
	v_writelane_b32 v252, s12, 7
	s_waitcnt vmcnt(4)
	v_lshlrev_b32_e32 v36, 16, v24
	v_and_b32_e32 v37, 0xffff0000, v24
	v_lshlrev_b32_e32 v38, 16, v25
	v_and_b32_e32 v39, 0xffff0000, v25
	buffer_load_dwordx4 v[24:27], v201, s[36:39], 0 offen sc1
	buffer_load_dwordx4 v[28:31], v206, s[36:39], 0 offen sc1
	global_load_dwordx4 v[50:53], v[40:41], off nt
	v_writelane_b32 v252, s13, 8
	v_writelane_b32 v252, s14, 9
	v_writelane_b32 v252, s15, 10
	s_lshl_b32 s12, s26, 10
	s_lshl_b32 s13, s25, 6
	s_and_b32 s12, s12, 0x6000
	s_ashr_i32 s14, s13, 31
	s_add_u32 s12, s12, s13
	s_addc_u32 s13, 0, s14
	s_lshl_b32 s14, s27, 4
	s_or_b32 s12, s12, s14
	v_or_b32_e32 v74, s12, v64
	s_lshl_b32 s12, s17, 6
	v_mov_b32_e32 v75, s13
	s_and_b32 s44, s12, 0x1c0
	v_lshlrev_b64 v[74:75], 9, v[74:75]
	v_lshl_add_u64 v[76:77], s[44:45], 0, v[194:195]
	v_lshl_add_u64 v[74:75], v[76:77], 0, v[74:75]
	v_lshlrev_b64 v[74:75], 1, v[74:75]
	v_lshl_add_u64 v[86:87], s[0:1], 0, v[74:75]
	v_lshl_add_u64 v[90:91], s[2:3], 0, v[74:75]
	v_lshl_add_u64 v[114:115], s[8:9], 0, v[74:75]
	v_lshl_add_u64 v[118:119], s[6:7], 0, v[74:75]
	buffer_load_dwordx4 v[40:43], v199, s[36:39], 0 offen sc1
	buffer_load_dwordx4 v[44:47], v207, s[36:39], 0 offen sc1
	v_lshlrev_b32_e32 v20, 16, v22
	v_and_b32_e32 v21, 0xffff0000, v22
	v_lshlrev_b32_e32 v22, 16, v23
	v_and_b32_e32 v23, 0xffff0000, v23
	buffer_load_dwordx4 v[66:69], v209, s[36:39], 0 offen sc1
	s_waitcnt vmcnt(3)
	v_lshlrev_b32_e32 v82, 16, v52
	v_and_b32_e32 v83, 0xffff0000, v52
	v_lshlrev_b32_e32 v84, 16, v53
	v_and_b32_e32 v85, 0xffff0000, v53
	buffer_load_dwordx4 v[52:55], v208, s[36:39], 0 offen sc1
	global_load_dwordx4 v[74:77], v[86:87], off nt
	global_load_dwordx4 v[78:81], v[90:91], off nt
	global_load_dwordx4 v[98:101], v[114:115], off nt
	global_load_dwordx4 v[94:97], v[118:119], off nt
	s_nop 0
	global_load_dwordx4 v[86:89], v[86:87], off offset:64 nt
	s_nop 0
	global_load_dwordx4 v[90:93], v[90:91], off offset:64 nt
	s_nop 0
	global_load_dwordx4 v[114:117], v[114:115], off offset:64 nt
	s_nop 0
	global_load_dwordx4 v[118:121], v[118:119], off offset:64 nt
	v_lshlrev_b32_e32 v48, 16, v50
	v_and_b32_e32 v49, 0xffff0000, v50
	v_lshlrev_b32_e32 v50, 16, v51
	v_and_b32_e32 v51, 0xffff0000, v51

; DI float bflo(unsigned w) { return __uint_as_float(w << 16); }
; DI float bfhi(unsigned w) { return __uint_as_float(w & 0xffff0000u); }
; DI void scanc_load(ScanCIn& o, const unsigned char* ws, GAS unsigned* flags, int item, int r16, int g, int l) {
;     ...
;     const unsigned char* rec1 = ws + WS_SC1 + ui * U1_BYTES; const unsigned char* rec2 = ws + WS_SC2 + ui * U2_BYTES;
;     const __amdgpu_buffer_rsrc_t srs = __builtin_amdgcn_make_buffer_rsrc((void*)(ws + WS_SCT + ui * 8192), 0, 8192, 0x00020000);
; #pragma unroll
;     for (int s = 0; s < 2; ++s) o.ra[s] = *(const bf16x8*)(rec1 + U_RPP + (size_t)((16 * it + r16) * 64 + 32 * s + 8 * g) * 2);
; #pragma unroll
;     for (int vt = 0; vt < 4; ++vt) { { const u32x2 yw = *(const u32x2*)(rec2 + U_YLT + (size_t)((16 * it + r16) * 64 + 32 * (vt >> 1) + 8 * g + 4 * (vt & 1)) * 2); o.yl[vt] = (f32x4){bflo(yw.x), bfhi(yw.x), bflo(yw.y), bfhi(yw.y)}; }
;         const int vrow = 32 * (vt >> 1) + 8 * (r16 >> 2) + 4 * (vt & 1) + (r16 & 3);
; #pragma unroll
;         for (int s = 0; s < 2; ++s) o.sb[vt][s] = __builtin_bit_cast(bf16x8, __builtin_amdgcn_raw_buffer_load_b128(srs, (int)((vrow * 64 + 32 * s + 8 * g) * 2), 0, 16)); }
;     { const bf16_t* SIr = (const bf16_t*)(ws + WS_SIR); const bf16_t* SIk = (const bf16_t*)(ws + WS_SIK); const bf16_t* V = (const bf16_t*)(ws + (l > 0 ? WS_V1 : WS_VF)); const bf16_t* Gb = (const bf16_t*)(ws + WS_G);
;       const int b = bh >> 3, h = bh & 7; const size_t o0 = ((size_t)b * SEQ + c * 64 + 16 * it + r16) * CW + h * 64 + 8 * g;
; #pragma unroll
;       for (int p = 0; p < 2; ++p) { o.pr[p] = *(const u32x4*)(SIr + o0 + 32 * p); o.pk[p] = *(const u32x4*)(SIk + o0 + 32 * p); o.pv[p] = *(const u32x4*)(V + o0 + 32 * p); o.pg[p] = *(const u32x4*)(Gb + o0 + 32 * p); } }
.LBB0_1240:
	s_lshl_b32 s14, s28, 7
	s_add_i32 s14, s14, s27
	s_ashr_i32 s15, s14, 31
	s_and_b32 s29, s29, 3
	s_lshl_b64 s[16:17], s[14:15], 14
	s_add_u32 s16, s94, s16
	s_addc_u32 s17, s95, s17
	s_lshl_b64 s[14:15], s[14:15], 13
	v_readlane_b32 s36, v252, 7
	s_add_u32 s36, s22, s14
	v_lshl_add_u32 v16, s29, 10, v197
	s_addc_u32 s30, s23, s15
	v_ashrrev_i32_e32 v17, 31, v16
	v_readlane_b32 s37, v252, 8
	s_add_u32 s14, s16, 0x1e202000
	v_lshlrev_b64 v[56:57], 1, v[16:17]
	s_addc_u32 s15, s17, 0
	v_lshl_add_u64 v[122:123], v[56:57], 0, 64
	s_and_b32 s37, s30, 0xffff
	v_lshl_add_u64 v[16:17], s[14:15], 0, v[56:57]
	v_lshl_add_u64 v[32:33], s[14:15], 0, v[122:123]
	s_add_u32 s14, s16, 0x16202000
	s_addc_u32 s15, s17, 0
	v_lshl_add_u64 v[56:57], s[14:15], 0, v[56:57]
	global_load_dwordx4 v[102:105], v[56:57], off nt
	v_readlane_b32 s38, v252, 9
	v_readlane_b32 s39, v252, 10
	v_lshl_add_u64 v[122:123], s[14:15], 0, v[122:123]
	global_load_dwordx4 v[16:19], v[16:17], off nt
	s_mov_b64 s[14:15], s[38:39]
	global_load_dwordx4 v[32:35], v[32:33], off nt
	s_nop 0
	buffer_load_dwordx4 v[56:59], v198, s[36:39], 0 offen sc1
	buffer_load_dwordx4 v[70:73], v200, s[36:39], 0 offen sc1
	v_writelane_b32 v252, s12, 7
	s_waitcnt vmcnt(4)
	v_lshlrev_b32_e32 v60, 16, v102
	v_and_b32_e32 v61, 0xffff0000, v102
	v_lshlrev_b32_e32 v62, 16, v103
	v_and_b32_e32 v63, 0xffff0000, v103
	v_lshlrev_b32_e32 v110, 16, v104
	v_and_b32_e32 v111, 0xffff0000, v104
	v_lshlrev_b32_e32 v112, 16, v105
	v_and_b32_e32 v113, 0xffff0000, v105
	buffer_load_dwordx4 v[102:105], v201, s[36:39], 0 offen sc1
	buffer_load_dwordx4 v[106:109], v206, s[36:39], 0 offen sc1
	global_load_dwordx4 v[132:135], v[122:123], off nt
	v_writelane_b32 v252, s13, 8
	v_writelane_b32 v252, s14, 9
	v_writelane_b32 v252, s15, 10
	s_lshl_b32 s14, s28, 10
	s_lshl_b32 s15, s27, 6
	s_and_b32 s14, s14, 0x6000
	s_ashr_i32 s16, s15, 31
	s_add_u32 s14, s14, s15
	s_addc_u32 s15, 0, s16
	s_lshl_b32 s16, s29, 4
	s_or_b32 s14, s14, s16
	v_or_b32_e32 v146, s14, v64
	s_lshl_b32 s14, s26, 6
	v_mov_b32_e32 v147, s15
	s_and_b32 s44, s14, 0x1c0
	v_lshlrev_b64 v[146:147], 9, v[146:147]
	v_lshl_add_u64 v[148:149], s[44:45], 0, v[194:195]
	v_lshl_add_u64 v[146:147], v[148:149], 0, v[146:147]
	v_lshlrev_b64 v[146:147], 1, v[146:147]
	v_lshl_add_u64 v[162:163], s[0:1], 0, v[146:147]
	v_lshl_add_u64 v[166:167], s[2:3], 0, v[146:147]
	v_lshl_add_u64 v[170:171], s[8:9], 0, v[146:147]
	v_lshl_add_u64 v[174:175], s[6:7], 0, v[146:147]
	buffer_load_dwordx4 v[122:125], v199, s[36:39], 0 offen sc1
	buffer_load_dwordx4 v[126:129], v207, s[36:39], 0 offen sc1
	buffer_load_dwordx4 v[138:141], v209, s[36:39], 0 offen sc1
	s_waitcnt vmcnt(3)
	v_lshlrev_b32_e32 v142, 16, v134
	v_and_b32_e32 v143, 0xffff0000, v134
	v_lshlrev_b32_e32 v144, 16, v135
	v_and_b32_e32 v145, 0xffff0000, v135
	buffer_load_dwordx4 v[134:137], v208, s[36:39], 0 offen sc1
	global_load_dwordx4 v[146:149], v[162:163], off nt
	global_load_dwordx4 v[150:153], v[166:167], off nt
	global_load_dwordx4 v[154:157], v[170:171], off nt
	global_load_dwordx4 v[158:161], v[174:175], off nt
	s_nop 0
	global_load_dwordx4 v[162:165], v[162:163], off offset:64 nt
	s_nop 0
	global_load_dwordx4 v[166:169], v[166:167], off offset:64 nt
	s_nop 0
	global_load_dwordx4 v[170:173], v[170:171], off offset:64 nt
	s_nop 0
	global_load_dwordx4 v[174:177], v[174:175], off offset:64 nt
	v_lshlrev_b32_e32 v130, 16, v132
	v_and_b32_e32 v131, 0xffff0000, v132
	v_lshlrev_b32_e32 v132, 16, v133
	v_and_b32_e32 v133, 0xffff0000, v133
